# baseline (speedup 1.0000x reference)
_Z5k_mixPKhPKfPhi:
	s_load_dwordx4 s[4:7], s[0:1], 0x0
	s_load_dwordx2 s[8:9], s[0:1], 0x10
	s_load_dword s10, s[0:1], 0x18
	v_lshl_or_b32 v1, s2, 8, v0
	v_lshlrev_b32_e32 v2, 4, v1
	v_lshrrev_b32_e32 v3, 5, v1
	s_mov_b32 s28, 0x41800000
	s_mov_b32 s30, 0x41000000
	s_waitcnt lgkmcnt(0)
	v_add_u32_e32 v3, s10, v3
	v_lshlrev_b32_e32 v3, 5, v3
	s_add_u32 s26, s6, 0x80000
	s_addc_u32 s27, s7, 0
	s_add_u32 s12, s4, 0x800000
	s_addc_u32 s13, s5, 0
	s_add_u32 s14, s12, 0x800000
	s_addc_u32 s15, s13, 0
	s_add_u32 s16, s14, 0x800000
	s_addc_u32 s17, s15, 0
	s_add_u32 s18, s16, 0x800000
	s_addc_u32 s19, s17, 0
	s_add_u32 s20, s18, 0x800000
	s_addc_u32 s21, s19, 0
	s_add_u32 s22, s20, 0x800000
	s_addc_u32 s23, s21, 0
	s_add_u32 s24, s22, 0x800000
	s_addc_u32 s25, s23, 0
	s_add_u32 s32, s8, 0x800000
	s_addc_u32 s33, s9, 0
	global_load_dwordx4 v[100:103], v3, s[6:7] nt
	global_load_dwordx4 v[104:107], v3, s[6:7] offset:16 nt
	global_load_dwordx4 v[108:111], v3, s[26:27] nt
	global_load_dwordx4 v[112:115], v3, s[26:27] offset:16 nt
	global_load_dwordx4 v[68:71], v2, s[4:5] nt
	global_load_dwordx4 v[72:75], v2, s[12:13] nt
	global_load_dwordx4 v[76:79], v2, s[14:15] nt
	global_load_dwordx4 v[80:83], v2, s[16:17] nt
	global_load_dwordx4 v[84:87], v2, s[18:19] nt
	global_load_dwordx4 v[88:91], v2, s[20:21] nt
	global_load_dwordx4 v[92:95], v2, s[22:23] nt
	global_load_dwordx4 v[96:99], v2, s[24:25] nt
	v_lshl_add_u32 v1, s10, 9, v2
	s_waitcnt vmcnt(8)
	v_pk_mul_f32 v[100:101], v[100:101], s[28:29] op_sel_hi:[1,0]
	v_pk_mul_f32 v[102:103], v[102:103], s[28:29] op_sel_hi:[1,0]
	v_pk_mul_f32 v[104:105], v[104:105], s[28:29] op_sel_hi:[1,0]
	v_pk_mul_f32 v[106:107], v[106:107], s[28:29] op_sel_hi:[1,0]
	v_pk_mul_f32 v[108:109], v[108:109], s[28:29] op_sel_hi:[1,0]
	v_pk_mul_f32 v[110:111], v[110:111], s[28:29] op_sel_hi:[1,0]
	v_pk_mul_f32 v[112:113], v[112:113], s[28:29] op_sel_hi:[1,0]
	v_pk_mul_f32 v[114:115], v[114:115], s[28:29] op_sel_hi:[1,0]
	s_waitcnt vmcnt(7)
	v_cvt_scalef32_pk_f32_fp4 v[116:117], v68, 1.0
	v_cvt_scalef32_pk_f32_fp4 v[118:119], v68, 1.0 op_sel:[1,0,0]
	v_cvt_scalef32_pk_f32_fp4 v[120:121], v68, 1.0 op_sel:[0,1,0]
	v_cvt_scalef32_pk_f32_fp4 v[122:123], v68, 1.0 op_sel:[1,1,0]
	v_pk_mul_f32 v[4:5], v[116:117], v[100:101] op_sel_hi:[1,0]
	v_pk_mul_f32 v[36:37], v[116:117], v[108:109] op_sel_hi:[1,0]
	v_pk_mul_f32 v[6:7], v[118:119], v[100:101] op_sel_hi:[1,0]
	v_pk_mul_f32 v[38:39], v[118:119], v[108:109] op_sel_hi:[1,0]
	v_pk_mul_f32 v[8:9], v[120:121], v[100:101] op_sel_hi:[1,0]
	v_pk_mul_f32 v[40:41], v[120:121], v[108:109] op_sel_hi:[1,0]
	v_pk_mul_f32 v[10:11], v[122:123], v[100:101] op_sel_hi:[1,0]
	v_pk_mul_f32 v[42:43], v[122:123], v[108:109] op_sel_hi:[1,0]
	v_cvt_scalef32_pk_f32_fp4 v[116:117], v69, 1.0
	v_cvt_scalef32_pk_f32_fp4 v[118:119], v69, 1.0 op_sel:[1,0,0]
	v_cvt_scalef32_pk_f32_fp4 v[120:121], v69, 1.0 op_sel:[0,1,0]
	v_cvt_scalef32_pk_f32_fp4 v[122:123], v69, 1.0 op_sel:[1,1,0]
	v_pk_mul_f32 v[12:13], v[116:117], v[100:101] op_sel_hi:[1,0]
	v_pk_mul_f32 v[44:45], v[116:117], v[108:109] op_sel_hi:[1,0]
	v_pk_mul_f32 v[14:15], v[118:119], v[100:101] op_sel_hi:[1,0]
	v_pk_mul_f32 v[46:47], v[118:119], v[108:109] op_sel_hi:[1,0]
	v_pk_mul_f32 v[16:17], v[120:121], v[100:101] op_sel_hi:[1,0]
	v_pk_mul_f32 v[48:49], v[120:121], v[108:109] op_sel_hi:[1,0]
	v_pk_mul_f32 v[18:19], v[122:123], v[100:101] op_sel_hi:[1,0]
	v_pk_mul_f32 v[50:51], v[122:123], v[108:109] op_sel_hi:[1,0]
	v_cvt_scalef32_pk_f32_fp4 v[116:117], v70, 1.0
	v_cvt_scalef32_pk_f32_fp4 v[118:119], v70, 1.0 op_sel:[1,0,0]
	v_cvt_scalef32_pk_f32_fp4 v[120:121], v70, 1.0 op_sel:[0,1,0]
	v_cvt_scalef32_pk_f32_fp4 v[122:123], v70, 1.0 op_sel:[1,1,0]
	v_pk_mul_f32 v[20:21], v[116:117], v[100:101] op_sel_hi:[1,0]
	v_pk_mul_f32 v[52:53], v[116:117], v[108:109] op_sel_hi:[1,0]
	v_pk_mul_f32 v[22:23], v[118:119], v[100:101] op_sel_hi:[1,0]
	v_pk_mul_f32 v[54:55], v[118:119], v[108:109] op_sel_hi:[1,0]
	v_pk_mul_f32 v[24:25], v[120:121], v[100:101] op_sel_hi:[1,0]
	v_pk_mul_f32 v[56:57], v[120:121], v[108:109] op_sel_hi:[1,0]
	v_pk_mul_f32 v[26:27], v[122:123], v[100:101] op_sel_hi:[1,0]
	v_pk_mul_f32 v[58:59], v[122:123], v[108:109] op_sel_hi:[1,0]
	v_cvt_scalef32_pk_f32_fp4 v[116:117], v71, 1.0
	v_cvt_scalef32_pk_f32_fp4 v[118:119], v71, 1.0 op_sel:[1,0,0]
	v_cvt_scalef32_pk_f32_fp4 v[120:121], v71, 1.0 op_sel:[0,1,0]
	v_cvt_scalef32_pk_f32_fp4 v[122:123], v71, 1.0 op_sel:[1,1,0]
	v_pk_mul_f32 v[28:29], v[116:117], v[100:101] op_sel_hi:[1,0]
	v_pk_mul_f32 v[60:61], v[116:117], v[108:109] op_sel_hi:[1,0]
	v_pk_mul_f32 v[30:31], v[118:119], v[100:101] op_sel_hi:[1,0]
	v_pk_mul_f32 v[62:63], v[118:119], v[108:109] op_sel_hi:[1,0]
	v_pk_mul_f32 v[32:33], v[120:121], v[100:101] op_sel_hi:[1,0]
	v_pk_mul_f32 v[64:65], v[120:121], v[108:109] op_sel_hi:[1,0]
	v_pk_mul_f32 v[34:35], v[122:123], v[100:101] op_sel_hi:[1,0]
	v_pk_mul_f32 v[66:67], v[122:123], v[108:109] op_sel_hi:[1,0]
	s_waitcnt vmcnt(6)
	v_cvt_scalef32_pk_f32_fp4 v[116:117], v72, 1.0
	v_cvt_scalef32_pk_f32_fp4 v[118:119], v72, 1.0 op_sel:[1,0,0]
	v_cvt_scalef32_pk_f32_fp4 v[120:121], v72, 1.0 op_sel:[0,1,0]
	v_cvt_scalef32_pk_f32_fp4 v[122:123], v72, 1.0 op_sel:[1,1,0]
	v_pk_fma_f32 v[4:5], v[116:117], v[100:101], v[4:5] op_sel:[0,1,0] op_sel_hi:[1,1,1]
	v_pk_fma_f32 v[36:37], v[116:117], v[108:109], v[36:37] op_sel:[0,1,0] op_sel_hi:[1,1,1]
	v_pk_fma_f32 v[6:7], v[118:119], v[100:101], v[6:7] op_sel:[0,1,0] op_sel_hi:[1,1,1]
	v_pk_fma_f32 v[38:39], v[118:119], v[108:109], v[38:39] op_sel:[0,1,0] op_sel_hi:[1,1,1]
	v_pk_fma_f32 v[8:9], v[120:121], v[100:101], v[8:9] op_sel:[0,1,0] op_sel_hi:[1,1,1]
	v_pk_fma_f32 v[40:41], v[120:121], v[108:109], v[40:41] op_sel:[0,1,0] op_sel_hi:[1,1,1]
	v_pk_fma_f32 v[10:11], v[122:123], v[100:101], v[10:11] op_sel:[0,1,0] op_sel_hi:[1,1,1]
	v_pk_fma_f32 v[42:43], v[122:123], v[108:109], v[42:43] op_sel:[0,1,0] op_sel_hi:[1,1,1]
	v_cvt_scalef32_pk_f32_fp4 v[116:117], v73, 1.0
	v_cvt_scalef32_pk_f32_fp4 v[118:119], v73, 1.0 op_sel:[1,0,0]
	v_cvt_scalef32_pk_f32_fp4 v[120:121], v73, 1.0 op_sel:[0,1,0]
	v_cvt_scalef32_pk_f32_fp4 v[122:123], v73, 1.0 op_sel:[1,1,0]
	v_pk_fma_f32 v[12:13], v[116:117], v[100:101], v[12:13] op_sel:[0,1,0] op_sel_hi:[1,1,1]
	v_pk_fma_f32 v[44:45], v[116:117], v[108:109], v[44:45] op_sel:[0,1,0] op_sel_hi:[1,1,1]
	v_pk_fma_f32 v[14:15], v[118:119], v[100:101], v[14:15] op_sel:[0,1,0] op_sel_hi:[1,1,1]
	v_pk_fma_f32 v[46:47], v[118:119], v[108:109], v[46:47] op_sel:[0,1,0] op_sel_hi:[1,1,1]
	v_pk_fma_f32 v[16:17], v[120:121], v[100:101], v[16:17] op_sel:[0,1,0] op_sel_hi:[1,1,1]
	v_pk_fma_f32 v[48:49], v[120:121], v[108:109], v[48:49] op_sel:[0,1,0] op_sel_hi:[1,1,1]
	v_pk_fma_f32 v[18:19], v[122:123], v[100:101], v[18:19] op_sel:[0,1,0] op_sel_hi:[1,1,1]
	v_pk_fma_f32 v[50:51], v[122:123], v[108:109], v[50:51] op_sel:[0,1,0] op_sel_hi:[1,1,1]
	v_cvt_scalef32_pk_f32_fp4 v[116:117], v74, 1.0
	v_cvt_scalef32_pk_f32_fp4 v[118:119], v74, 1.0 op_sel:[1,0,0]
	v_cvt_scalef32_pk_f32_fp4 v[120:121], v74, 1.0 op_sel:[0,1,0]
	v_cvt_scalef32_pk_f32_fp4 v[122:123], v74, 1.0 op_sel:[1,1,0]
	v_pk_fma_f32 v[20:21], v[116:117], v[100:101], v[20:21] op_sel:[0,1,0] op_sel_hi:[1,1,1]
	v_pk_fma_f32 v[52:53], v[116:117], v[108:109], v[52:53] op_sel:[0,1,0] op_sel_hi:[1,1,1]
	v_pk_fma_f32 v[22:23], v[118:119], v[100:101], v[22:23] op_sel:[0,1,0] op_sel_hi:[1,1,1]
	v_pk_fma_f32 v[54:55], v[118:119], v[108:109], v[54:55] op_sel:[0,1,0] op_sel_hi:[1,1,1]
	v_pk_fma_f32 v[24:25], v[120:121], v[100:101], v[24:25] op_sel:[0,1,0] op_sel_hi:[1,1,1]
	v_pk_fma_f32 v[56:57], v[120:121], v[108:109], v[56:57] op_sel:[0,1,0] op_sel_hi:[1,1,1]
	v_pk_fma_f32 v[26:27], v[122:123], v[100:101], v[26:27] op_sel:[0,1,0] op_sel_hi:[1,1,1]
	v_pk_fma_f32 v[58:59], v[122:123], v[108:109], v[58:59] op_sel:[0,1,0] op_sel_hi:[1,1,1]
	v_cvt_scalef32_pk_f32_fp4 v[116:117], v75, 1.0
	v_cvt_scalef32_pk_f32_fp4 v[118:119], v75, 1.0 op_sel:[1,0,0]
	v_cvt_scalef32_pk_f32_fp4 v[120:121], v75, 1.0 op_sel:[0,1,0]
	v_cvt_scalef32_pk_f32_fp4 v[122:123], v75, 1.0 op_sel:[1,1,0]
	v_pk_fma_f32 v[28:29], v[116:117], v[100:101], v[28:29] op_sel:[0,1,0] op_sel_hi:[1,1,1]
	v_pk_fma_f32 v[60:61], v[116:117], v[108:109], v[60:61] op_sel:[0,1,0] op_sel_hi:[1,1,1]
	v_pk_fma_f32 v[30:31], v[118:119], v[100:101], v[30:31] op_sel:[0,1,0] op_sel_hi:[1,1,1]
	v_pk_fma_f32 v[62:63], v[118:119], v[108:109], v[62:63] op_sel:[0,1,0] op_sel_hi:[1,1,1]
	v_pk_fma_f32 v[32:33], v[120:121], v[100:101], v[32:33] op_sel:[0,1,0] op_sel_hi:[1,1,1]
	v_pk_fma_f32 v[64:65], v[120:121], v[108:109], v[64:65] op_sel:[0,1,0] op_sel_hi:[1,1,1]
	v_pk_fma_f32 v[34:35], v[122:123], v[100:101], v[34:35] op_sel:[0,1,0] op_sel_hi:[1,1,1]
	v_pk_fma_f32 v[66:67], v[122:123], v[108:109], v[66:67] op_sel:[0,1,0] op_sel_hi:[1,1,1]
	s_waitcnt vmcnt(5)
	v_cvt_scalef32_pk_f32_fp4 v[116:117], v76, 1.0
	v_cvt_scalef32_pk_f32_fp4 v[118:119], v76, 1.0 op_sel:[1,0,0]
	v_cvt_scalef32_pk_f32_fp4 v[120:121], v76, 1.0 op_sel:[0,1,0]
	v_cvt_scalef32_pk_f32_fp4 v[122:123], v76, 1.0 op_sel:[1,1,0]
	v_pk_fma_f32 v[4:5], v[116:117], v[102:103], v[4:5] op_sel_hi:[1,0,1]
	v_pk_fma_f32 v[36:37], v[116:117], v[110:111], v[36:37] op_sel_hi:[1,0,1]
	v_pk_fma_f32 v[6:7], v[118:119], v[102:103], v[6:7] op_sel_hi:[1,0,1]
	v_pk_fma_f32 v[38:39], v[118:119], v[110:111], v[38:39] op_sel_hi:[1,0,1]
	v_pk_fma_f32 v[8:9], v[120:121], v[102:103], v[8:9] op_sel_hi:[1,0,1]
	v_pk_fma_f32 v[40:41], v[120:121], v[110:111], v[40:41] op_sel_hi:[1,0,1]
	v_pk_fma_f32 v[10:11], v[122:123], v[102:103], v[10:11] op_sel_hi:[1,0,1]
	v_pk_fma_f32 v[42:43], v[122:123], v[110:111], v[42:43] op_sel_hi:[1,0,1]
	v_cvt_scalef32_pk_f32_fp4 v[116:117], v77, 1.0
	v_cvt_scalef32_pk_f32_fp4 v[118:119], v77, 1.0 op_sel:[1,0,0]
	v_cvt_scalef32_pk_f32_fp4 v[120:121], v77, 1.0 op_sel:[0,1,0]
	v_cvt_scalef32_pk_f32_fp4 v[122:123], v77, 1.0 op_sel:[1,1,0]
	v_pk_fma_f32 v[12:13], v[116:117], v[102:103], v[12:13] op_sel_hi:[1,0,1]
	v_pk_fma_f32 v[44:45], v[116:117], v[110:111], v[44:45] op_sel_hi:[1,0,1]
	v_pk_fma_f32 v[14:15], v[118:119], v[102:103], v[14:15] op_sel_hi:[1,0,1]
	v_pk_fma_f32 v[46:47], v[118:119], v[110:111], v[46:47] op_sel_hi:[1,0,1]
	v_pk_fma_f32 v[16:17], v[120:121], v[102:103], v[16:17] op_sel_hi:[1,0,1]
	v_pk_fma_f32 v[48:49], v[120:121], v[110:111], v[48:49] op_sel_hi:[1,0,1]
	v_pk_fma_f32 v[18:19], v[122:123], v[102:103], v[18:19] op_sel_hi:[1,0,1]
	v_pk_fma_f32 v[50:51], v[122:123], v[110:111], v[50:51] op_sel_hi:[1,0,1]
	v_cvt_scalef32_pk_f32_fp4 v[116:117], v78, 1.0
	v_cvt_scalef32_pk_f32_fp4 v[118:119], v78, 1.0 op_sel:[1,0,0]
	v_cvt_scalef32_pk_f32_fp4 v[120:121], v78, 1.0 op_sel:[0,1,0]
	v_cvt_scalef32_pk_f32_fp4 v[122:123], v78, 1.0 op_sel:[1,1,0]
	v_pk_fma_f32 v[20:21], v[116:117], v[102:103], v[20:21] op_sel_hi:[1,0,1]
	v_pk_fma_f32 v[52:53], v[116:117], v[110:111], v[52:53] op_sel_hi:[1,0,1]
	v_pk_fma_f32 v[22:23], v[118:119], v[102:103], v[22:23] op_sel_hi:[1,0,1]
	v_pk_fma_f32 v[54:55], v[118:119], v[110:111], v[54:55] op_sel_hi:[1,0,1]
	v_pk_fma_f32 v[24:25], v[120:121], v[102:103], v[24:25] op_sel_hi:[1,0,1]
	v_pk_fma_f32 v[56:57], v[120:121], v[110:111], v[56:57] op_sel_hi:[1,0,1]
	v_pk_fma_f32 v[26:27], v[122:123], v[102:103], v[26:27] op_sel_hi:[1,0,1]
	v_pk_fma_f32 v[58:59], v[122:123], v[110:111], v[58:59] op_sel_hi:[1,0,1]
	v_cvt_scalef32_pk_f32_fp4 v[116:117], v79, 1.0
	v_cvt_scalef32_pk_f32_fp4 v[118:119], v79, 1.0 op_sel:[1,0,0]
	v_cvt_scalef32_pk_f32_fp4 v[120:121], v79, 1.0 op_sel:[0,1,0]
	v_cvt_scalef32_pk_f32_fp4 v[122:123], v79, 1.0 op_sel:[1,1,0]
	v_pk_fma_f32 v[28:29], v[116:117], v[102:103], v[28:29] op_sel_hi:[1,0,1]
	v_pk_fma_f32 v[60:61], v[116:117], v[110:111], v[60:61] op_sel_hi:[1,0,1]
	v_pk_fma_f32 v[30:31], v[118:119], v[102:103], v[30:31] op_sel_hi:[1,0,1]
	v_pk_fma_f32 v[62:63], v[118:119], v[110:111], v[62:63] op_sel_hi:[1,0,1]
	v_pk_fma_f32 v[32:33], v[120:121], v[102:103], v[32:33] op_sel_hi:[1,0,1]
	v_pk_fma_f32 v[64:65], v[120:121], v[110:111], v[64:65] op_sel_hi:[1,0,1]
	v_pk_fma_f32 v[34:35], v[122:123], v[102:103], v[34:35] op_sel_hi:[1,0,1]
	v_pk_fma_f32 v[66:67], v[122:123], v[110:111], v[66:67] op_sel_hi:[1,0,1]
	s_waitcnt vmcnt(4)
	v_cvt_scalef32_pk_f32_fp4 v[116:117], v80, 1.0
	v_cvt_scalef32_pk_f32_fp4 v[118:119], v80, 1.0 op_sel:[1,0,0]
	v_cvt_scalef32_pk_f32_fp4 v[120:121], v80, 1.0 op_sel:[0,1,0]
	v_cvt_scalef32_pk_f32_fp4 v[122:123], v80, 1.0 op_sel:[1,1,0]
	v_pk_fma_f32 v[4:5], v[116:117], v[102:103], v[4:5] op_sel:[0,1,0] op_sel_hi:[1,1,1]
	v_pk_fma_f32 v[36:37], v[116:117], v[110:111], v[36:37] op_sel:[0,1,0] op_sel_hi:[1,1,1]
	v_pk_fma_f32 v[6:7], v[118:119], v[102:103], v[6:7] op_sel:[0,1,0] op_sel_hi:[1,1,1]
	v_pk_fma_f32 v[38:39], v[118:119], v[110:111], v[38:39] op_sel:[0,1,0] op_sel_hi:[1,1,1]
	v_pk_fma_f32 v[8:9], v[120:121], v[102:103], v[8:9] op_sel:[0,1,0] op_sel_hi:[1,1,1]
	v_pk_fma_f32 v[40:41], v[120:121], v[110:111], v[40:41] op_sel:[0,1,0] op_sel_hi:[1,1,1]
	v_pk_fma_f32 v[10:11], v[122:123], v[102:103], v[10:11] op_sel:[0,1,0] op_sel_hi:[1,1,1]
	v_pk_fma_f32 v[42:43], v[122:123], v[110:111], v[42:43] op_sel:[0,1,0] op_sel_hi:[1,1,1]
	v_cvt_scalef32_pk_f32_fp4 v[116:117], v81, 1.0
	v_cvt_scalef32_pk_f32_fp4 v[118:119], v81, 1.0 op_sel:[1,0,0]
	v_cvt_scalef32_pk_f32_fp4 v[120:121], v81, 1.0 op_sel:[0,1,0]
	v_cvt_scalef32_pk_f32_fp4 v[122:123], v81, 1.0 op_sel:[1,1,0]
	v_pk_fma_f32 v[12:13], v[116:117], v[102:103], v[12:13] op_sel:[0,1,0] op_sel_hi:[1,1,1]
	v_pk_fma_f32 v[44:45], v[116:117], v[110:111], v[44:45] op_sel:[0,1,0] op_sel_hi:[1,1,1]
	v_pk_fma_f32 v[14:15], v[118:119], v[102:103], v[14:15] op_sel:[0,1,0] op_sel_hi:[1,1,1]
	v_pk_fma_f32 v[46:47], v[118:119], v[110:111], v[46:47] op_sel:[0,1,0] op_sel_hi:[1,1,1]
	v_pk_fma_f32 v[16:17], v[120:121], v[102:103], v[16:17] op_sel:[0,1,0] op_sel_hi:[1,1,1]
	v_pk_fma_f32 v[48:49], v[120:121], v[110:111], v[48:49] op_sel:[0,1,0] op_sel_hi:[1,1,1]
	v_pk_fma_f32 v[18:19], v[122:123], v[102:103], v[18:19] op_sel:[0,1,0] op_sel_hi:[1,1,1]
	v_pk_fma_f32 v[50:51], v[122:123], v[110:111], v[50:51] op_sel:[0,1,0] op_sel_hi:[1,1,1]
	v_cvt_scalef32_pk_f32_fp4 v[116:117], v82, 1.0
	v_cvt_scalef32_pk_f32_fp4 v[118:119], v82, 1.0 op_sel:[1,0,0]
	v_cvt_scalef32_pk_f32_fp4 v[120:121], v82, 1.0 op_sel:[0,1,0]
	v_cvt_scalef32_pk_f32_fp4 v[122:123], v82, 1.0 op_sel:[1,1,0]
	v_pk_fma_f32 v[20:21], v[116:117], v[102:103], v[20:21] op_sel:[0,1,0] op_sel_hi:[1,1,1]
	v_pk_fma_f32 v[52:53], v[116:117], v[110:111], v[52:53] op_sel:[0,1,0] op_sel_hi:[1,1,1]
	v_pk_fma_f32 v[22:23], v[118:119], v[102:103], v[22:23] op_sel:[0,1,0] op_sel_hi:[1,1,1]
	v_pk_fma_f32 v[54:55], v[118:119], v[110:111], v[54:55] op_sel:[0,1,0] op_sel_hi:[1,1,1]
	v_pk_fma_f32 v[24:25], v[120:121], v[102:103], v[24:25] op_sel:[0,1,0] op_sel_hi:[1,1,1]
	v_pk_fma_f32 v[56:57], v[120:121], v[110:111], v[56:57] op_sel:[0,1,0] op_sel_hi:[1,1,1]
	v_pk_fma_f32 v[26:27], v[122:123], v[102:103], v[26:27] op_sel:[0,1,0] op_sel_hi:[1,1,1]
	v_pk_fma_f32 v[58:59], v[122:123], v[110:111], v[58:59] op_sel:[0,1,0] op_sel_hi:[1,1,1]
	v_cvt_scalef32_pk_f32_fp4 v[116:117], v83, 1.0
	v_cvt_scalef32_pk_f32_fp4 v[118:119], v83, 1.0 op_sel:[1,0,0]
	v_cvt_scalef32_pk_f32_fp4 v[120:121], v83, 1.0 op_sel:[0,1,0]
	v_cvt_scalef32_pk_f32_fp4 v[122:123], v83, 1.0 op_sel:[1,1,0]
	v_pk_fma_f32 v[28:29], v[116:117], v[102:103], v[28:29] op_sel:[0,1,0] op_sel_hi:[1,1,1]
	v_pk_fma_f32 v[60:61], v[116:117], v[110:111], v[60:61] op_sel:[0,1,0] op_sel_hi:[1,1,1]
	v_pk_fma_f32 v[30:31], v[118:119], v[102:103], v[30:31] op_sel:[0,1,0] op_sel_hi:[1,1,1]
	v_pk_fma_f32 v[62:63], v[118:119], v[110:111], v[62:63] op_sel:[0,1,0] op_sel_hi:[1,1,1]
	v_pk_fma_f32 v[32:33], v[120:121], v[102:103], v[32:33] op_sel:[0,1,0] op_sel_hi:[1,1,1]
	v_pk_fma_f32 v[64:65], v[120:121], v[110:111], v[64:65] op_sel:[0,1,0] op_sel_hi:[1,1,1]
	v_pk_fma_f32 v[34:35], v[122:123], v[102:103], v[34:35] op_sel:[0,1,0] op_sel_hi:[1,1,1]
	v_pk_fma_f32 v[66:67], v[122:123], v[110:111], v[66:67] op_sel:[0,1,0] op_sel_hi:[1,1,1]
	s_waitcnt vmcnt(3)
	v_cvt_scalef32_pk_f32_fp4 v[116:117], v84, 1.0
	v_cvt_scalef32_pk_f32_fp4 v[118:119], v84, 1.0 op_sel:[1,0,0]
	v_cvt_scalef32_pk_f32_fp4 v[120:121], v84, 1.0 op_sel:[0,1,0]
	v_cvt_scalef32_pk_f32_fp4 v[122:123], v84, 1.0 op_sel:[1,1,0]
	v_pk_fma_f32 v[4:5], v[116:117], v[104:105], v[4:5] op_sel_hi:[1,0,1]
	v_pk_fma_f32 v[36:37], v[116:117], v[112:113], v[36:37] op_sel_hi:[1,0,1]
	v_pk_fma_f32 v[6:7], v[118:119], v[104:105], v[6:7] op_sel_hi:[1,0,1]
	v_pk_fma_f32 v[38:39], v[118:119], v[112:113], v[38:39] op_sel_hi:[1,0,1]
	v_pk_fma_f32 v[8:9], v[120:121], v[104:105], v[8:9] op_sel_hi:[1,0,1]
	v_pk_fma_f32 v[40:41], v[120:121], v[112:113], v[40:41] op_sel_hi:[1,0,1]
	v_pk_fma_f32 v[10:11], v[122:123], v[104:105], v[10:11] op_sel_hi:[1,0,1]
	v_pk_fma_f32 v[42:43], v[122:123], v[112:113], v[42:43] op_sel_hi:[1,0,1]
	v_cvt_scalef32_pk_f32_fp4 v[116:117], v85, 1.0
	v_cvt_scalef32_pk_f32_fp4 v[118:119], v85, 1.0 op_sel:[1,0,0]
	v_cvt_scalef32_pk_f32_fp4 v[120:121], v85, 1.0 op_sel:[0,1,0]
	v_cvt_scalef32_pk_f32_fp4 v[122:123], v85, 1.0 op_sel:[1,1,0]
	v_pk_fma_f32 v[12:13], v[116:117], v[104:105], v[12:13] op_sel_hi:[1,0,1]
	v_pk_fma_f32 v[44:45], v[116:117], v[112:113], v[44:45] op_sel_hi:[1,0,1]
	v_pk_fma_f32 v[14:15], v[118:119], v[104:105], v[14:15] op_sel_hi:[1,0,1]
	v_pk_fma_f32 v[46:47], v[118:119], v[112:113], v[46:47] op_sel_hi:[1,0,1]
	v_pk_fma_f32 v[16:17], v[120:121], v[104:105], v[16:17] op_sel_hi:[1,0,1]
	v_pk_fma_f32 v[48:49], v[120:121], v[112:113], v[48:49] op_sel_hi:[1,0,1]
	v_pk_fma_f32 v[18:19], v[122:123], v[104:105], v[18:19] op_sel_hi:[1,0,1]
	v_pk_fma_f32 v[50:51], v[122:123], v[112:113], v[50:51] op_sel_hi:[1,0,1]
	v_cvt_scalef32_pk_f32_fp4 v[116:117], v86, 1.0
	v_cvt_scalef32_pk_f32_fp4 v[118:119], v86, 1.0 op_sel:[1,0,0]
	v_cvt_scalef32_pk_f32_fp4 v[120:121], v86, 1.0 op_sel:[0,1,0]
	v_cvt_scalef32_pk_f32_fp4 v[122:123], v86, 1.0 op_sel:[1,1,0]
	v_pk_fma_f32 v[20:21], v[116:117], v[104:105], v[20:21] op_sel_hi:[1,0,1]
	v_pk_fma_f32 v[52:53], v[116:117], v[112:113], v[52:53] op_sel_hi:[1,0,1]
	v_pk_fma_f32 v[22:23], v[118:119], v[104:105], v[22:23] op_sel_hi:[1,0,1]
	v_pk_fma_f32 v[54:55], v[118:119], v[112:113], v[54:55] op_sel_hi:[1,0,1]
	v_pk_fma_f32 v[24:25], v[120:121], v[104:105], v[24:25] op_sel_hi:[1,0,1]
	v_pk_fma_f32 v[56:57], v[120:121], v[112:113], v[56:57] op_sel_hi:[1,0,1]
	v_pk_fma_f32 v[26:27], v[122:123], v[104:105], v[26:27] op_sel_hi:[1,0,1]
	v_pk_fma_f32 v[58:59], v[122:123], v[112:113], v[58:59] op_sel_hi:[1,0,1]
	v_cvt_scalef32_pk_f32_fp4 v[116:117], v87, 1.0
	v_cvt_scalef32_pk_f32_fp4 v[118:119], v87, 1.0 op_sel:[1,0,0]
	v_cvt_scalef32_pk_f32_fp4 v[120:121], v87, 1.0 op_sel:[0,1,0]
	v_cvt_scalef32_pk_f32_fp4 v[122:123], v87, 1.0 op_sel:[1,1,0]
	v_pk_fma_f32 v[28:29], v[116:117], v[104:105], v[28:29] op_sel_hi:[1,0,1]
	v_pk_fma_f32 v[60:61], v[116:117], v[112:113], v[60:61] op_sel_hi:[1,0,1]
	v_pk_fma_f32 v[30:31], v[118:119], v[104:105], v[30:31] op_sel_hi:[1,0,1]
	v_pk_fma_f32 v[62:63], v[118:119], v[112:113], v[62:63] op_sel_hi:[1,0,1]
	v_pk_fma_f32 v[32:33], v[120:121], v[104:105], v[32:33] op_sel_hi:[1,0,1]
	v_pk_fma_f32 v[64:65], v[120:121], v[112:113], v[64:65] op_sel_hi:[1,0,1]
	v_pk_fma_f32 v[34:35], v[122:123], v[104:105], v[34:35] op_sel_hi:[1,0,1]
	v_pk_fma_f32 v[66:67], v[122:123], v[112:113], v[66:67] op_sel_hi:[1,0,1]
	s_waitcnt vmcnt(2)
	v_cvt_scalef32_pk_f32_fp4 v[116:117], v88, 1.0
	v_cvt_scalef32_pk_f32_fp4 v[118:119], v88, 1.0 op_sel:[1,0,0]
	v_cvt_scalef32_pk_f32_fp4 v[120:121], v88, 1.0 op_sel:[0,1,0]
	v_cvt_scalef32_pk_f32_fp4 v[122:123], v88, 1.0 op_sel:[1,1,0]
	v_pk_fma_f32 v[4:5], v[116:117], v[104:105], v[4:5] op_sel:[0,1,0] op_sel_hi:[1,1,1]
	v_pk_fma_f32 v[36:37], v[116:117], v[112:113], v[36:37] op_sel:[0,1,0] op_sel_hi:[1,1,1]
	v_pk_fma_f32 v[6:7], v[118:119], v[104:105], v[6:7] op_sel:[0,1,0] op_sel_hi:[1,1,1]
	v_pk_fma_f32 v[38:39], v[118:119], v[112:113], v[38:39] op_sel:[0,1,0] op_sel_hi:[1,1,1]
	v_pk_fma_f32 v[8:9], v[120:121], v[104:105], v[8:9] op_sel:[0,1,0] op_sel_hi:[1,1,1]
	v_pk_fma_f32 v[40:41], v[120:121], v[112:113], v[40:41] op_sel:[0,1,0] op_sel_hi:[1,1,1]
	v_pk_fma_f32 v[10:11], v[122:123], v[104:105], v[10:11] op_sel:[0,1,0] op_sel_hi:[1,1,1]
	v_pk_fma_f32 v[42:43], v[122:123], v[112:113], v[42:43] op_sel:[0,1,0] op_sel_hi:[1,1,1]
	v_cvt_scalef32_pk_f32_fp4 v[116:117], v89, 1.0
	v_cvt_scalef32_pk_f32_fp4 v[118:119], v89, 1.0 op_sel:[1,0,0]
	v_cvt_scalef32_pk_f32_fp4 v[120:121], v89, 1.0 op_sel:[0,1,0]
	v_cvt_scalef32_pk_f32_fp4 v[122:123], v89, 1.0 op_sel:[1,1,0]
	v_pk_fma_f32 v[12:13], v[116:117], v[104:105], v[12:13] op_sel:[0,1,0] op_sel_hi:[1,1,1]
	v_pk_fma_f32 v[44:45], v[116:117], v[112:113], v[44:45] op_sel:[0,1,0] op_sel_hi:[1,1,1]
	v_pk_fma_f32 v[14:15], v[118:119], v[104:105], v[14:15] op_sel:[0,1,0] op_sel_hi:[1,1,1]
	v_pk_fma_f32 v[46:47], v[118:119], v[112:113], v[46:47] op_sel:[0,1,0] op_sel_hi:[1,1,1]
	v_pk_fma_f32 v[16:17], v[120:121], v[104:105], v[16:17] op_sel:[0,1,0] op_sel_hi:[1,1,1]
	v_pk_fma_f32 v[48:49], v[120:121], v[112:113], v[48:49] op_sel:[0,1,0] op_sel_hi:[1,1,1]
	v_pk_fma_f32 v[18:19], v[122:123], v[104:105], v[18:19] op_sel:[0,1,0] op_sel_hi:[1,1,1]
	v_pk_fma_f32 v[50:51], v[122:123], v[112:113], v[50:51] op_sel:[0,1,0] op_sel_hi:[1,1,1]
	v_cvt_scalef32_pk_f32_fp4 v[116:117], v90, 1.0
	v_cvt_scalef32_pk_f32_fp4 v[118:119], v90, 1.0 op_sel:[1,0,0]
	v_cvt_scalef32_pk_f32_fp4 v[120:121], v90, 1.0 op_sel:[0,1,0]
	v_cvt_scalef32_pk_f32_fp4 v[122:123], v90, 1.0 op_sel:[1,1,0]
	v_pk_fma_f32 v[20:21], v[116:117], v[104:105], v[20:21] op_sel:[0,1,0] op_sel_hi:[1,1,1]
	v_pk_fma_f32 v[52:53], v[116:117], v[112:113], v[52:53] op_sel:[0,1,0] op_sel_hi:[1,1,1]
	v_pk_fma_f32 v[22:23], v[118:119], v[104:105], v[22:23] op_sel:[0,1,0] op_sel_hi:[1,1,1]
	v_pk_fma_f32 v[54:55], v[118:119], v[112:113], v[54:55] op_sel:[0,1,0] op_sel_hi:[1,1,1]
	v_pk_fma_f32 v[24:25], v[120:121], v[104:105], v[24:25] op_sel:[0,1,0] op_sel_hi:[1,1,1]
	v_pk_fma_f32 v[56:57], v[120:121], v[112:113], v[56:57] op_sel:[0,1,0] op_sel_hi:[1,1,1]
	v_pk_fma_f32 v[26:27], v[122:123], v[104:105], v[26:27] op_sel:[0,1,0] op_sel_hi:[1,1,1]
	v_pk_fma_f32 v[58:59], v[122:123], v[112:113], v[58:59] op_sel:[0,1,0] op_sel_hi:[1,1,1]
	v_cvt_scalef32_pk_f32_fp4 v[116:117], v91, 1.0
	v_cvt_scalef32_pk_f32_fp4 v[118:119], v91, 1.0 op_sel:[1,0,0]
	v_cvt_scalef32_pk_f32_fp4 v[120:121], v91, 1.0 op_sel:[0,1,0]
	v_cvt_scalef32_pk_f32_fp4 v[122:123], v91, 1.0 op_sel:[1,1,0]
	v_pk_fma_f32 v[28:29], v[116:117], v[104:105], v[28:29] op_sel:[0,1,0] op_sel_hi:[1,1,1]
	v_pk_fma_f32 v[60:61], v[116:117], v[112:113], v[60:61] op_sel:[0,1,0] op_sel_hi:[1,1,1]
	v_pk_fma_f32 v[30:31], v[118:119], v[104:105], v[30:31] op_sel:[0,1,0] op_sel_hi:[1,1,1]
	v_pk_fma_f32 v[62:63], v[118:119], v[112:113], v[62:63] op_sel:[0,1,0] op_sel_hi:[1,1,1]
	v_pk_fma_f32 v[32:33], v[120:121], v[104:105], v[32:33] op_sel:[0,1,0] op_sel_hi:[1,1,1]
	v_pk_fma_f32 v[64:65], v[120:121], v[112:113], v[64:65] op_sel:[0,1,0] op_sel_hi:[1,1,1]
	v_pk_fma_f32 v[34:35], v[122:123], v[104:105], v[34:35] op_sel:[0,1,0] op_sel_hi:[1,1,1]
	v_pk_fma_f32 v[66:67], v[122:123], v[112:113], v[66:67] op_sel:[0,1,0] op_sel_hi:[1,1,1]
	s_waitcnt vmcnt(1)
	v_cvt_scalef32_pk_f32_fp4 v[116:117], v92, 1.0
	v_cvt_scalef32_pk_f32_fp4 v[118:119], v92, 1.0 op_sel:[1,0,0]
	v_cvt_scalef32_pk_f32_fp4 v[120:121], v92, 1.0 op_sel:[0,1,0]
	v_cvt_scalef32_pk_f32_fp4 v[122:123], v92, 1.0 op_sel:[1,1,0]
	v_pk_fma_f32 v[4:5], v[116:117], v[106:107], v[4:5] op_sel_hi:[1,0,1]
	v_pk_fma_f32 v[36:37], v[116:117], v[114:115], v[36:37] op_sel_hi:[1,0,1]
	v_pk_fma_f32 v[6:7], v[118:119], v[106:107], v[6:7] op_sel_hi:[1,0,1]
	v_pk_fma_f32 v[38:39], v[118:119], v[114:115], v[38:39] op_sel_hi:[1,0,1]
	v_pk_fma_f32 v[8:9], v[120:121], v[106:107], v[8:9] op_sel_hi:[1,0,1]
	v_pk_fma_f32 v[40:41], v[120:121], v[114:115], v[40:41] op_sel_hi:[1,0,1]
	v_pk_fma_f32 v[10:11], v[122:123], v[106:107], v[10:11] op_sel_hi:[1,0,1]
	v_pk_fma_f32 v[42:43], v[122:123], v[114:115], v[42:43] op_sel_hi:[1,0,1]
	v_cvt_scalef32_pk_f32_fp4 v[116:117], v93, 1.0
	v_cvt_scalef32_pk_f32_fp4 v[118:119], v93, 1.0 op_sel:[1,0,0]
	v_cvt_scalef32_pk_f32_fp4 v[120:121], v93, 1.0 op_sel:[0,1,0]
	v_cvt_scalef32_pk_f32_fp4 v[122:123], v93, 1.0 op_sel:[1,1,0]
	v_pk_fma_f32 v[12:13], v[116:117], v[106:107], v[12:13] op_sel_hi:[1,0,1]
	v_pk_fma_f32 v[44:45], v[116:117], v[114:115], v[44:45] op_sel_hi:[1,0,1]
	v_pk_fma_f32 v[14:15], v[118:119], v[106:107], v[14:15] op_sel_hi:[1,0,1]
	v_pk_fma_f32 v[46:47], v[118:119], v[114:115], v[46:47] op_sel_hi:[1,0,1]
	v_pk_fma_f32 v[16:17], v[120:121], v[106:107], v[16:17] op_sel_hi:[1,0,1]
	v_pk_fma_f32 v[48:49], v[120:121], v[114:115], v[48:49] op_sel_hi:[1,0,1]
	v_pk_fma_f32 v[18:19], v[122:123], v[106:107], v[18:19] op_sel_hi:[1,0,1]
	v_pk_fma_f32 v[50:51], v[122:123], v[114:115], v[50:51] op_sel_hi:[1,0,1]
	v_cvt_scalef32_pk_f32_fp4 v[116:117], v94, 1.0
	v_cvt_scalef32_pk_f32_fp4 v[118:119], v94, 1.0 op_sel:[1,0,0]
	v_cvt_scalef32_pk_f32_fp4 v[120:121], v94, 1.0 op_sel:[0,1,0]
	v_cvt_scalef32_pk_f32_fp4 v[122:123], v94, 1.0 op_sel:[1,1,0]
	v_pk_fma_f32 v[20:21], v[116:117], v[106:107], v[20:21] op_sel_hi:[1,0,1]
	v_pk_fma_f32 v[52:53], v[116:117], v[114:115], v[52:53] op_sel_hi:[1,0,1]
	v_pk_fma_f32 v[22:23], v[118:119], v[106:107], v[22:23] op_sel_hi:[1,0,1]
	v_pk_fma_f32 v[54:55], v[118:119], v[114:115], v[54:55] op_sel_hi:[1,0,1]
	v_pk_fma_f32 v[24:25], v[120:121], v[106:107], v[24:25] op_sel_hi:[1,0,1]
	v_pk_fma_f32 v[56:57], v[120:121], v[114:115], v[56:57] op_sel_hi:[1,0,1]
	v_pk_fma_f32 v[26:27], v[122:123], v[106:107], v[26:27] op_sel_hi:[1,0,1]
	v_pk_fma_f32 v[58:59], v[122:123], v[114:115], v[58:59] op_sel_hi:[1,0,1]
	v_cvt_scalef32_pk_f32_fp4 v[116:117], v95, 1.0
	v_cvt_scalef32_pk_f32_fp4 v[118:119], v95, 1.0 op_sel:[1,0,0]
	v_cvt_scalef32_pk_f32_fp4 v[120:121], v95, 1.0 op_sel:[0,1,0]
	v_cvt_scalef32_pk_f32_fp4 v[122:123], v95, 1.0 op_sel:[1,1,0]
	v_pk_fma_f32 v[28:29], v[116:117], v[106:107], v[28:29] op_sel_hi:[1,0,1]
	v_pk_fma_f32 v[60:61], v[116:117], v[114:115], v[60:61] op_sel_hi:[1,0,1]
	v_pk_fma_f32 v[30:31], v[118:119], v[106:107], v[30:31] op_sel_hi:[1,0,1]
	v_pk_fma_f32 v[62:63], v[118:119], v[114:115], v[62:63] op_sel_hi:[1,0,1]
	v_pk_fma_f32 v[32:33], v[120:121], v[106:107], v[32:33] op_sel_hi:[1,0,1]
	v_pk_fma_f32 v[64:65], v[120:121], v[114:115], v[64:65] op_sel_hi:[1,0,1]
	v_pk_fma_f32 v[34:35], v[122:123], v[106:107], v[34:35] op_sel_hi:[1,0,1]
	v_pk_fma_f32 v[66:67], v[122:123], v[114:115], v[66:67] op_sel_hi:[1,0,1]
	s_waitcnt vmcnt(0)
	v_cvt_scalef32_pk_f32_fp4 v[116:117], v96, 1.0
	v_cvt_scalef32_pk_f32_fp4 v[118:119], v96, 1.0 op_sel:[1,0,0]
	v_cvt_scalef32_pk_f32_fp4 v[120:121], v96, 1.0 op_sel:[0,1,0]
	v_cvt_scalef32_pk_f32_fp4 v[122:123], v96, 1.0 op_sel:[1,1,0]
	v_pk_fma_f32 v[4:5], v[116:117], v[106:107], v[4:5] op_sel:[0,1,0] op_sel_hi:[1,1,1]
	v_pk_fma_f32 v[36:37], v[116:117], v[114:115], v[36:37] op_sel:[0,1,0] op_sel_hi:[1,1,1]
	v_pk_fma_f32 v[6:7], v[118:119], v[106:107], v[6:7] op_sel:[0,1,0] op_sel_hi:[1,1,1]
	v_pk_fma_f32 v[38:39], v[118:119], v[114:115], v[38:39] op_sel:[0,1,0] op_sel_hi:[1,1,1]
	v_pk_fma_f32 v[8:9], v[120:121], v[106:107], v[8:9] op_sel:[0,1,0] op_sel_hi:[1,1,1]
	v_pk_fma_f32 v[40:41], v[120:121], v[114:115], v[40:41] op_sel:[0,1,0] op_sel_hi:[1,1,1]
	v_pk_fma_f32 v[10:11], v[122:123], v[106:107], v[10:11] op_sel:[0,1,0] op_sel_hi:[1,1,1]
	v_pk_fma_f32 v[42:43], v[122:123], v[114:115], v[42:43] op_sel:[0,1,0] op_sel_hi:[1,1,1]
	v_cvt_scalef32_pk_f32_fp4 v[116:117], v97, 1.0
	v_cvt_scalef32_pk_f32_fp4 v[118:119], v97, 1.0 op_sel:[1,0,0]
	v_cvt_scalef32_pk_f32_fp4 v[120:121], v97, 1.0 op_sel:[0,1,0]
	v_cvt_scalef32_pk_f32_fp4 v[122:123], v97, 1.0 op_sel:[1,1,0]
	v_pk_fma_f32 v[12:13], v[116:117], v[106:107], v[12:13] op_sel:[0,1,0] op_sel_hi:[1,1,1]
	v_pk_fma_f32 v[44:45], v[116:117], v[114:115], v[44:45] op_sel:[0,1,0] op_sel_hi:[1,1,1]
	v_pk_fma_f32 v[14:15], v[118:119], v[106:107], v[14:15] op_sel:[0,1,0] op_sel_hi:[1,1,1]
	v_pk_fma_f32 v[46:47], v[118:119], v[114:115], v[46:47] op_sel:[0,1,0] op_sel_hi:[1,1,1]
	v_pk_fma_f32 v[16:17], v[120:121], v[106:107], v[16:17] op_sel:[0,1,0] op_sel_hi:[1,1,1]
	v_pk_fma_f32 v[48:49], v[120:121], v[114:115], v[48:49] op_sel:[0,1,0] op_sel_hi:[1,1,1]
	v_pk_fma_f32 v[18:19], v[122:123], v[106:107], v[18:19] op_sel:[0,1,0] op_sel_hi:[1,1,1]
	v_pk_fma_f32 v[50:51], v[122:123], v[114:115], v[50:51] op_sel:[0,1,0] op_sel_hi:[1,1,1]
	v_cvt_scalef32_pk_f32_fp4 v[116:117], v98, 1.0
	v_cvt_scalef32_pk_f32_fp4 v[118:119], v98, 1.0 op_sel:[1,0,0]
	v_cvt_scalef32_pk_f32_fp4 v[120:121], v98, 1.0 op_sel:[0,1,0]
	v_cvt_scalef32_pk_f32_fp4 v[122:123], v98, 1.0 op_sel:[1,1,0]
	v_pk_fma_f32 v[20:21], v[116:117], v[106:107], v[20:21] op_sel:[0,1,0] op_sel_hi:[1,1,1]
	v_pk_fma_f32 v[52:53], v[116:117], v[114:115], v[52:53] op_sel:[0,1,0] op_sel_hi:[1,1,1]
	v_pk_fma_f32 v[22:23], v[118:119], v[106:107], v[22:23] op_sel:[0,1,0] op_sel_hi:[1,1,1]
	v_pk_fma_f32 v[54:55], v[118:119], v[114:115], v[54:55] op_sel:[0,1,0] op_sel_hi:[1,1,1]
	v_pk_fma_f32 v[24:25], v[120:121], v[106:107], v[24:25] op_sel:[0,1,0] op_sel_hi:[1,1,1]
	v_pk_fma_f32 v[56:57], v[120:121], v[114:115], v[56:57] op_sel:[0,1,0] op_sel_hi:[1,1,1]
	v_pk_fma_f32 v[26:27], v[122:123], v[106:107], v[26:27] op_sel:[0,1,0] op_sel_hi:[1,1,1]
	v_pk_fma_f32 v[58:59], v[122:123], v[114:115], v[58:59] op_sel:[0,1,0] op_sel_hi:[1,1,1]
	v_cvt_scalef32_pk_f32_fp4 v[116:117], v99, 1.0
	v_cvt_scalef32_pk_f32_fp4 v[118:119], v99, 1.0 op_sel:[1,0,0]
	v_cvt_scalef32_pk_f32_fp4 v[120:121], v99, 1.0 op_sel:[0,1,0]
	v_cvt_scalef32_pk_f32_fp4 v[122:123], v99, 1.0 op_sel:[1,1,0]
	v_pk_fma_f32 v[28:29], v[116:117], v[106:107], v[28:29] op_sel:[0,1,0] op_sel_hi:[1,1,1]
	v_pk_fma_f32 v[60:61], v[116:117], v[114:115], v[60:61] op_sel:[0,1,0] op_sel_hi:[1,1,1]
	v_pk_fma_f32 v[30:31], v[118:119], v[106:107], v[30:31] op_sel:[0,1,0] op_sel_hi:[1,1,1]
	v_pk_fma_f32 v[62:63], v[118:119], v[114:115], v[62:63] op_sel:[0,1,0] op_sel_hi:[1,1,1]
	v_pk_fma_f32 v[32:33], v[120:121], v[106:107], v[32:33] op_sel:[0,1,0] op_sel_hi:[1,1,1]
	v_pk_fma_f32 v[64:65], v[120:121], v[114:115], v[64:65] op_sel:[0,1,0] op_sel_hi:[1,1,1]
	v_pk_fma_f32 v[34:35], v[122:123], v[106:107], v[34:35] op_sel:[0,1,0] op_sel_hi:[1,1,1]
	v_pk_fma_f32 v[66:67], v[122:123], v[114:115], v[66:67] op_sel:[0,1,0] op_sel_hi:[1,1,1]
	v_cvt_scalef32_pk_fp4_f32 v68, v4, v5, s30
	v_cvt_scalef32_pk_fp4_f32 v68, v6, v7, s30 op_sel:[0,0,1,0]
	v_cvt_scalef32_pk_fp4_f32 v68, v8, v9, s30 op_sel:[0,0,0,1]
	v_cvt_scalef32_pk_fp4_f32 v68, v10, v11, s30 op_sel:[0,0,1,1]
	v_cvt_scalef32_pk_fp4_f32 v69, v12, v13, s30
	v_cvt_scalef32_pk_fp4_f32 v69, v14, v15, s30 op_sel:[0,0,1,0]
	v_cvt_scalef32_pk_fp4_f32 v69, v16, v17, s30 op_sel:[0,0,0,1]
	v_cvt_scalef32_pk_fp4_f32 v69, v18, v19, s30 op_sel:[0,0,1,1]
	v_cvt_scalef32_pk_fp4_f32 v70, v20, v21, s30
	v_cvt_scalef32_pk_fp4_f32 v70, v22, v23, s30 op_sel:[0,0,1,0]
	v_cvt_scalef32_pk_fp4_f32 v70, v24, v25, s30 op_sel:[0,0,0,1]
	v_cvt_scalef32_pk_fp4_f32 v70, v26, v27, s30 op_sel:[0,0,1,1]
	v_cvt_scalef32_pk_fp4_f32 v71, v28, v29, s30
	v_cvt_scalef32_pk_fp4_f32 v71, v30, v31, s30 op_sel:[0,0,1,0]
	v_cvt_scalef32_pk_fp4_f32 v71, v32, v33, s30 op_sel:[0,0,0,1]
	v_cvt_scalef32_pk_fp4_f32 v71, v34, v35, s30 op_sel:[0,0,1,1]
	v_cvt_scalef32_pk_fp4_f32 v72, v36, v37, s30
	v_cvt_scalef32_pk_fp4_f32 v72, v38, v39, s30 op_sel:[0,0,1,0]
	v_cvt_scalef32_pk_fp4_f32 v72, v40, v41, s30 op_sel:[0,0,0,1]
	v_cvt_scalef32_pk_fp4_f32 v72, v42, v43, s30 op_sel:[0,0,1,1]
	v_cvt_scalef32_pk_fp4_f32 v73, v44, v45, s30
	v_cvt_scalef32_pk_fp4_f32 v73, v46, v47, s30 op_sel:[0,0,1,0]
	v_cvt_scalef32_pk_fp4_f32 v73, v48, v49, s30 op_sel:[0,0,0,1]
	v_cvt_scalef32_pk_fp4_f32 v73, v50, v51, s30 op_sel:[0,0,1,1]
	v_cvt_scalef32_pk_fp4_f32 v74, v52, v53, s30
	v_cvt_scalef32_pk_fp4_f32 v74, v54, v55, s30 op_sel:[0,0,1,0]
	v_cvt_scalef32_pk_fp4_f32 v74, v56, v57, s30 op_sel:[0,0,0,1]
	v_cvt_scalef32_pk_fp4_f32 v74, v58, v59, s30 op_sel:[0,0,1,1]
	v_cvt_scalef32_pk_fp4_f32 v75, v60, v61, s30
	v_cvt_scalef32_pk_fp4_f32 v75, v62, v63, s30 op_sel:[0,0,1,0]
	v_cvt_scalef32_pk_fp4_f32 v75, v64, v65, s30 op_sel:[0,0,0,1]
	v_cvt_scalef32_pk_fp4_f32 v75, v66, v67, s30 op_sel:[0,0,1,1]
	global_store_dwordx4 v1, v[68:71], s[8:9]
	global_store_dwordx4 v1, v[72:75], s[32:33]
	s_endpgm

_Z7k_finalPKfS0_Pf:
	s_load_dwordx4 s[4:7], s[0:1], 0x0
	s_load_dwordx2 s[8:9], s[0:1], 0x10
	s_lshl_b32 s0, s2, 8
	v_or_b32_e32 v4, s0, v0
	v_ashrrev_i32_e32 v5, 31, v4
	v_lshlrev_b64 v[0:1], 5, v[4:5]
	s_bfe_i32 s0, s2, 0x10017
	s_waitcnt lgkmcnt(0)
	v_lshl_add_u64 v[6:7], s[4:5], 0, v[0:1]
	s_lshr_b32 s0, s0, 18
	global_load_dwordx4 v[12:15], v[6:7], off nt
	global_load_dwordx4 v[0:3], v[6:7], off offset:16 nt
	v_add_u32_e32 v6, s0, v4
	v_ashrrev_i32_e32 v6, 14, v6
	v_ashrrev_i32_e32 v7, 31, v6
	v_lshl_add_u64 v[6:7], v[6:7], 2, s[6:7]
	global_load_dword v10, v[6:7], off
	s_waitcnt vmcnt(2)
	v_mov_b32_e32 v6, v12
	s_waitcnt vmcnt(1)
	v_mov_b32_e32 v7, v0
	v_mov_b32_e32 v0, v13
	v_mov_b32_e32 v8, v14
	v_mov_b32_e32 v9, v2
	v_mov_b32_e32 v2, v15
	v_pk_add_f32 v[0:1], v[6:7], v[0:1]
	v_pk_add_f32 v[2:3], v[8:9], v[2:3]
	s_nop 0
	v_pk_add_f32 v[0:1], v[0:1], v[2:3]
	s_nop 0
	v_add_f32_e32 v0, v0, v1
	s_waitcnt vmcnt(0)
	v_add_f32_e32 v0, v10, v0
	v_mul_f32_e32 v0, 0xbfb8aa3b, v0
	v_exp_f32_e32 v0, v0
	s_nop 0
	v_add_f32_e32 v0, 1.0, v0
	v_div_scale_f32 v1, s[0:1], v0, v0, 1.0
	v_rcp_f32_e32 v2, v1
	v_div_scale_f32 v3, vcc, 1.0, v0, 1.0
	v_fma_f32 v6, -v1, v2, 1.0
	v_fmac_f32_e32 v2, v6, v2
	v_mul_f32_e32 v6, v3, v2
	v_fma_f32 v7, -v1, v6, v3
	v_fmac_f32_e32 v6, v7, v2
	v_fma_f32 v1, -v1, v6, v3
	v_div_fmas_f32 v1, v1, v2, v6
	v_div_fixup_f32 v2, v1, v0, 1.0
	v_lshl_add_u64 v[0:1], v[4:5], 2, s[8:9]
	global_store_dword v[0:1], v2, off
	s_endpgm
